# baseline (speedup 1.0000x reference)
.LBB2_54:
	v_lshlrev_b32_e32 v3, 2, v0
	v_and_b32_e32 v10, 31, v0
	v_lshrrev_b32_e32 v0, 8, v0
	v_or_b32_e32 v0, s33, v0
	s_movk_i32 s4, 0x880
	s_waitcnt lgkmcnt(0)
	v_mov_b64_e32 v[4:5], s[72:73]
	v_mad_u64_u32 v[4:5], s[0:1], v0, s4, v[4:5]
	v_and_b32_e32 v0, 0x3fc, v3
	v_cmp_lt_i32_e32 vcc, v180, v181
	v_lshlrev_b32_e32 v6, 1, v0
	v_mov_b32_e32 v7, 0
	v_cndmask_b32_e32 v0, v179, v180, vcc
	v_lshlrev_b32_e32 v0, 2, v0
	ds_bpermute_b32 v0, v0, v2
	v_lshl_add_u64 v[4:5], v[4:5], 0, v[6:7]
	s_movk_i32 s0, 0x1000
	s_waitcnt vmcnt(1)
	v_cvt_pk_f16_f32 v8, v134, v135
	v_cvt_pk_f16_f32 v9, v136, v137
	s_waitcnt lgkmcnt(0)
	v_add_f32_e32 v0, v2, v0
	v_div_scale_f32 v6, s[2:3], v0, v0, 1.0
	v_rcp_f32_e32 v11, v6
	v_add_co_u32_e32 v2, vcc, s0, v4
	global_store_dwordx2 v[4:5], v[8:9], off
	s_waitcnt vmcnt(1)
	v_cvt_pk_f16_f32 v8, v130, v131
	v_cvt_pk_f16_f32 v9, v132, v133
	v_addc_co_u32_e32 v3, vcc, 0, v5, vcc
	global_store_dwordx2 v[2:3], v[8:9], off offset:256
	v_fma_f32 v2, -v6, v11, 1.0
	v_fmac_f32_e32 v11, v2, v11
	v_div_scale_f32 v2, vcc, 1.0, v0, 1.0
	v_mul_f32_e32 v3, v2, v11
	v_fma_f32 v4, -v6, v3, v2
	v_fmac_f32_e32 v3, v4, v11
	v_fma_f32 v2, -v6, v3, v2
	v_div_fmas_f32 v2, v2, v11, v3
	s_movk_i32 s0, 0x1200
	v_div_fixup_f32 v0, v2, v0, 1.0
	v_mad_u32_u24 v14, v177, s0, 0
	v_mul_u32_u24_e32 v2, 0x90, v10
	v_lshlrev_b32_e32 v3, 3, v171
	v_add3_u32 v6, v14, v2, v3
	v_pk_mul_f32 v[2:3], v[0:1], v[98:99] op_sel_hi:[0,1]
	v_pk_mul_f32 v[4:5], v[0:1], v[100:101] op_sel_hi:[0,1]
	v_cvt_pk_f16_f32 v2, v2, v3
	v_cvt_pk_f16_f32 v3, v4, v5
	v_pk_mul_f32 v[4:5], v[0:1], v[66:67] op_sel_hi:[0,1]
	v_pk_mul_f32 v[8:9], v[0:1], v[68:69] op_sel_hi:[0,1]
	v_cvt_pk_f16_f32 v4, v4, v5
	v_cvt_pk_f16_f32 v5, v8, v9
	v_pk_mul_f32 v[8:9], v[0:1], v[102:103] op_sel_hi:[0,1]
	v_pk_mul_f32 v[10:11], v[0:1], v[104:105] op_sel_hi:[0,1]
	v_cvt_pk_f16_f32 v8, v8, v9
	v_cvt_pk_f16_f32 v9, v10, v11
	v_pk_mul_f32 v[10:11], v[0:1], v[70:71] op_sel_hi:[0,1]
	v_pk_mul_f32 v[12:13], v[0:1], v[72:73] op_sel_hi:[0,1]
	s_waitcnt vmcnt(0)
	s_barrier
	v_cvt_pk_f16_f32 v10, v10, v11
	v_cvt_pk_f16_f32 v11, v12, v13
	ds_write2_b64 v6, v[2:3], v[8:9] offset1:2
	ds_write2_b64 v6, v[4:5], v[10:11] offset0:8 offset1:10
	v_pk_mul_f32 v[2:3], v[0:1], v[106:107] op_sel_hi:[0,1]
	v_pk_mul_f32 v[4:5], v[0:1], v[108:109] op_sel_hi:[0,1]
	v_cvt_pk_f16_f32 v2, v2, v3
	v_cvt_pk_f16_f32 v3, v4, v5
	v_pk_mul_f32 v[4:5], v[0:1], v[74:75] op_sel_hi:[0,1]
	v_pk_mul_f32 v[8:9], v[0:1], v[76:77] op_sel_hi:[0,1]
	v_cvt_pk_f16_f32 v4, v4, v5
	v_cvt_pk_f16_f32 v5, v8, v9
	v_pk_mul_f32 v[8:9], v[0:1], v[110:111] op_sel_hi:[0,1]
	v_pk_mul_f32 v[10:11], v[0:1], v[112:113] op_sel_hi:[0,1]
	v_cvt_pk_f16_f32 v8, v8, v9
	v_cvt_pk_f16_f32 v9, v10, v11
	v_pk_mul_f32 v[10:11], v[0:1], v[78:79] op_sel_hi:[0,1]
	v_pk_mul_f32 v[12:13], v[0:1], v[80:81] op_sel_hi:[0,1]
	v_lshlrev_b32_e32 v0, 5, v176
	v_cvt_pk_f16_f32 v10, v10, v11
	v_cvt_pk_f16_f32 v11, v12, v13
	ds_write2_b64 v6, v[2:3], v[8:9] offset0:4 offset1:6
	ds_write2_b64 v6, v[4:5], v[10:11] offset0:12 offset1:14
	v_lshl_or_b32 v0, s68, 11, v0
	v_mov_b64_e32 v[2:3], s[70:71]
	s_lshl_b32 s0, s66, 7
	v_lshrrev_b32_e32 v8, 3, v1
	s_mov_b32 s1, 0
	v_mad_i64_i32 v[2:3], s[2:3], v0, s4, v[2:3]
	s_and_b32 s0, s0, 0x780
	v_and_b32_e32 v6, 0x70, v170
	v_mul_u32_u24_e32 v0, 0x90, v8
	s_waitcnt lgkmcnt(0)
	v_lshl_add_u64 v[2:3], v[2:3], 0, s[0:1]
	v_add3_u32 v12, v14, v6, v0
	v_lshl_add_u64 v[4:5], v[2:3], 0, v[6:7]
	ds_read_b128 v[0:3], v12
	v_mul_u32_u24_e32 v6, 0x440, v8
	v_lshlrev_b32_e32 v6, 1, v6
	v_lshl_add_u64 v[8:9], v[4:5], 0, v[6:7]
	ds_read_b128 v[4:7], v12 offset:1152
	s_movk_i32 s0, 0x4000
	s_waitcnt lgkmcnt(1)
	global_store_dwordx4 v[8:9], v[0:3], off nt
	s_nop 1
	v_add_co_u32_e32 v0, vcc, s0, v8
	s_nop 1
	v_addc_co_u32_e32 v1, vcc, 0, v9, vcc
	s_waitcnt lgkmcnt(0)
	global_store_dwordx4 v[0:1], v[4:7], off offset:1024 nt
	ds_read_b128 v[0:3], v12 offset:2304
	ds_read_b128 v[4:7], v12 offset:3456
	v_add_co_u32_e32 v10, vcc, 0x8000, v8
	s_nop 1
	v_addc_co_u32_e32 v11, vcc, 0, v9, vcc
	s_waitcnt lgkmcnt(1)
	global_store_dwordx4 v[10:11], v[0:3], off offset:2048 nt
	s_nop 1
	v_add_co_u32_e32 v0, vcc, 0xc000, v8
	s_nop 1
	v_addc_co_u32_e32 v1, vcc, 0, v9, vcc
	s_waitcnt lgkmcnt(0)
	global_store_dwordx4 v[0:1], v[4:7], off offset:3072 nt
	s_endpgm
